# agg gather ring 10 rows deep (was 8): two more row slots in the registers freed by the relation-bias removal
# baseline (speedup 1.0000x reference)
.Lagg_inner:
	s_sub_u32 s16, s14, s15
	s_min_u32 s16, s16, 10
	s_cmp_ge_u32 s16, 10
	s_cbranch_scc1 .Lagg_ld9
	s_cmp_ge_u32 s16, 9
	s_cbranch_scc1 .Lagg_ld8
	s_cmp_ge_u32 s16, 8
	s_cbranch_scc1 .Lagg_ld7
	s_cmp_ge_u32 s16, 7
	s_cbranch_scc1 .Lagg_ld6
	s_cmp_ge_u32 s16, 6
	s_cbranch_scc1 .Lagg_ld5
	s_cmp_ge_u32 s16, 5
	s_cbranch_scc1 .Lagg_ld4
	s_cmp_ge_u32 s16, 4
	s_cbranch_scc1 .Lagg_ld3
	s_cmp_ge_u32 s16, 3
	s_cbranch_scc1 .Lagg_ld2
	s_cmp_ge_u32 s16, 2
	s_cbranch_scc1 .Lagg_ld1
	s_branch .Lagg_ld0
.Lagg_ld9:
	s_add_u32 s17, s15, 9
	v_readlane_b32 s28, v6, s17
	s_mul_i32 s29, s28, 0x220
	s_add_u32 s58, s26, s29
	s_addc_u32 s59, s27, 0
	global_load_dwordx2 v[58:59], v8, s[58:59]
	global_load_dword v31, v20, s[58:59] offset:512
.Lagg_ld8:
	s_add_u32 s17, s15, 8
	v_readlane_b32 s28, v6, s17
	s_mul_i32 s29, s28, 0x220
	s_add_u32 s56, s26, s29
	s_addc_u32 s57, s27, 0
	global_load_dwordx2 v[56:57], v8, s[56:57]
	global_load_dword v30, v20, s[56:57] offset:512

.Lagg_chk:
	s_sub_u32 s17, s14, s15
	s_cmp_ge_u32 s17, 20
	s_cbranch_scc1 .Lagg_pipe
	s_cmp_ge_u32 s16, 10
	s_cbranch_scc1 .Lagg_ac9
	s_cmp_ge_u32 s16, 9
	s_cbranch_scc1 .Lagg_ac8
	s_cmp_ge_u32 s16, 8
	s_cbranch_scc1 .Lagg_ac7
	s_cmp_ge_u32 s16, 7
	s_cbranch_scc1 .Lagg_ac6
	s_cmp_ge_u32 s16, 6
	s_cbranch_scc1 .Lagg_ac5
	s_cmp_ge_u32 s16, 5
	s_cbranch_scc1 .Lagg_ac4
	s_cmp_ge_u32 s16, 4
	s_cbranch_scc1 .Lagg_ac3
	s_cmp_ge_u32 s16, 3
	s_cbranch_scc1 .Lagg_ac2
	s_cmp_ge_u32 s16, 2
	s_cbranch_scc1 .Lagg_ac1
	s_branch .Lagg_ac0
.Lagg_ac9:
	s_waitcnt vmcnt(18)
	v_cvt_f32_i32_sdwa v2, sext(v58) dst_sel:DWORD dst_unused:UNUSED_PAD src0_sel:BYTE_0
	v_cvt_f32_i32_sdwa v3, sext(v58) dst_sel:DWORD dst_unused:UNUSED_PAD src0_sel:BYTE_1
	v_cvt_f32_i32_sdwa v22, sext(v58) dst_sel:DWORD dst_unused:UNUSED_PAD src0_sel:BYTE_2
	v_cvt_f32_i32_sdwa v23, sext(v58) dst_sel:DWORD dst_unused:UNUSED_PAD src0_sel:BYTE_3
	v_cvt_f32_i32_sdwa v26, sext(v59) dst_sel:DWORD dst_unused:UNUSED_PAD src0_sel:BYTE_0
	v_cvt_f32_i32_sdwa v27, sext(v59) dst_sel:DWORD dst_unused:UNUSED_PAD src0_sel:BYTE_1
	v_cvt_f32_i32_sdwa v28, sext(v59) dst_sel:DWORD dst_unused:UNUSED_PAD src0_sel:BYTE_2
	v_cvt_f32_i32_sdwa v29, sext(v59) dst_sel:DWORD dst_unused:UNUSED_PAD src0_sel:BYTE_3
	v_pk_fma_f32 v[16:17], v[30:31], v[2:3], v[16:17] op_sel:[1,0,0] op_sel_hi:[1,1,1]
	v_pk_fma_f32 v[14:15], v[30:31], v[22:23], v[14:15] op_sel:[1,0,0] op_sel_hi:[1,1,1]
	v_pk_fma_f32 v[12:13], v[30:31], v[26:27], v[12:13] op_sel:[1,0,0] op_sel_hi:[1,1,1]
	v_pk_fma_f32 v[10:11], v[30:31], v[28:29], v[10:11] op_sel:[1,0,0] op_sel_hi:[1,1,1]
.Lagg_ac8:
	s_waitcnt vmcnt(16)
	v_cvt_f32_i32_sdwa v2, sext(v56) dst_sel:DWORD dst_unused:UNUSED_PAD src0_sel:BYTE_0
	v_cvt_f32_i32_sdwa v3, sext(v56) dst_sel:DWORD dst_unused:UNUSED_PAD src0_sel:BYTE_1
	v_cvt_f32_i32_sdwa v22, sext(v56) dst_sel:DWORD dst_unused:UNUSED_PAD src0_sel:BYTE_2
	v_cvt_f32_i32_sdwa v23, sext(v56) dst_sel:DWORD dst_unused:UNUSED_PAD src0_sel:BYTE_3
	v_cvt_f32_i32_sdwa v26, sext(v57) dst_sel:DWORD dst_unused:UNUSED_PAD src0_sel:BYTE_0
	v_cvt_f32_i32_sdwa v27, sext(v57) dst_sel:DWORD dst_unused:UNUSED_PAD src0_sel:BYTE_1
	v_cvt_f32_i32_sdwa v28, sext(v57) dst_sel:DWORD dst_unused:UNUSED_PAD src0_sel:BYTE_2
	v_cvt_f32_i32_sdwa v29, sext(v57) dst_sel:DWORD dst_unused:UNUSED_PAD src0_sel:BYTE_3
	v_pk_fma_f32 v[16:17], v[30:31], v[2:3], v[16:17] op_sel_hi:[0,1,1]
	v_pk_fma_f32 v[14:15], v[30:31], v[22:23], v[14:15] op_sel_hi:[0,1,1]
	v_pk_fma_f32 v[12:13], v[30:31], v[26:27], v[12:13] op_sel_hi:[0,1,1]
	v_pk_fma_f32 v[10:11], v[30:31], v[28:29], v[10:11] op_sel_hi:[0,1,1]

.Lagg_ac0:
	s_waitcnt vmcnt(0)
	v_cvt_f32_i32_sdwa v2, sext(v40) dst_sel:DWORD dst_unused:UNUSED_PAD src0_sel:BYTE_0
	v_cvt_f32_i32_sdwa v3, sext(v40) dst_sel:DWORD dst_unused:UNUSED_PAD src0_sel:BYTE_1
	v_cvt_f32_i32_sdwa v22, sext(v40) dst_sel:DWORD dst_unused:UNUSED_PAD src0_sel:BYTE_2
	v_cvt_f32_i32_sdwa v23, sext(v40) dst_sel:DWORD dst_unused:UNUSED_PAD src0_sel:BYTE_3
	v_cvt_f32_i32_sdwa v26, sext(v41) dst_sel:DWORD dst_unused:UNUSED_PAD src0_sel:BYTE_0
	v_cvt_f32_i32_sdwa v27, sext(v41) dst_sel:DWORD dst_unused:UNUSED_PAD src0_sel:BYTE_1
	v_cvt_f32_i32_sdwa v28, sext(v41) dst_sel:DWORD dst_unused:UNUSED_PAD src0_sel:BYTE_2
	v_cvt_f32_i32_sdwa v29, sext(v41) dst_sel:DWORD dst_unused:UNUSED_PAD src0_sel:BYTE_3
	v_pk_fma_f32 v[16:17], v[32:33], v[2:3], v[16:17] op_sel_hi:[0,1,1]
	v_pk_fma_f32 v[14:15], v[32:33], v[22:23], v[14:15] op_sel_hi:[0,1,1]
	v_pk_fma_f32 v[12:13], v[32:33], v[26:27], v[12:13] op_sel_hi:[0,1,1]
	v_pk_fma_f32 v[10:11], v[32:33], v[28:29], v[10:11] op_sel_hi:[0,1,1]
	s_add_u32 s15, s15, 10
	s_cmp_lt_u32 s15, s14
	s_cbranch_scc1 .Lagg_inner
	s_add_u32 s3, s3, 64
	s_cmp_lt_u32 s3, s2
	s_cbranch_scc1 .Lagg_outer
	s_branch .LBB1_26
.Lagg_pipe:
	s_waitcnt vmcnt(18)
	v_cvt_f32_i32_sdwa v2, sext(v58) dst_sel:DWORD dst_unused:UNUSED_PAD src0_sel:BYTE_0
	v_cvt_f32_i32_sdwa v3, sext(v58) dst_sel:DWORD dst_unused:UNUSED_PAD src0_sel:BYTE_1
	v_cvt_f32_i32_sdwa v22, sext(v58) dst_sel:DWORD dst_unused:UNUSED_PAD src0_sel:BYTE_2
	v_cvt_f32_i32_sdwa v23, sext(v58) dst_sel:DWORD dst_unused:UNUSED_PAD src0_sel:BYTE_3
	v_cvt_f32_i32_sdwa v26, sext(v59) dst_sel:DWORD dst_unused:UNUSED_PAD src0_sel:BYTE_0
	v_cvt_f32_i32_sdwa v27, sext(v59) dst_sel:DWORD dst_unused:UNUSED_PAD src0_sel:BYTE_1
	v_cvt_f32_i32_sdwa v28, sext(v59) dst_sel:DWORD dst_unused:UNUSED_PAD src0_sel:BYTE_2
	v_cvt_f32_i32_sdwa v29, sext(v59) dst_sel:DWORD dst_unused:UNUSED_PAD src0_sel:BYTE_3
	v_pk_fma_f32 v[16:17], v[30:31], v[2:3], v[16:17] op_sel:[1,0,0] op_sel_hi:[1,1,1]
	v_pk_fma_f32 v[14:15], v[30:31], v[22:23], v[14:15] op_sel:[1,0,0] op_sel_hi:[1,1,1]
	v_pk_fma_f32 v[12:13], v[30:31], v[26:27], v[12:13] op_sel:[1,0,0] op_sel_hi:[1,1,1]
	v_pk_fma_f32 v[10:11], v[30:31], v[28:29], v[10:11] op_sel:[1,0,0] op_sel_hi:[1,1,1]
	s_add_u32 s17, s15, 19
	v_readlane_b32 s28, v6, s17
	s_mul_i32 s29, s28, 0x220
	s_add_u32 s58, s26, s29
	s_addc_u32 s59, s27, 0
	global_load_dwordx2 v[58:59], v8, s[58:59]
	global_load_dword v31, v20, s[58:59] offset:512
	s_waitcnt vmcnt(18)
	v_cvt_f32_i32_sdwa v2, sext(v56) dst_sel:DWORD dst_unused:UNUSED_PAD src0_sel:BYTE_0
	v_cvt_f32_i32_sdwa v3, sext(v56) dst_sel:DWORD dst_unused:UNUSED_PAD src0_sel:BYTE_1
	v_cvt_f32_i32_sdwa v22, sext(v56) dst_sel:DWORD dst_unused:UNUSED_PAD src0_sel:BYTE_2
	v_cvt_f32_i32_sdwa v23, sext(v56) dst_sel:DWORD dst_unused:UNUSED_PAD src0_sel:BYTE_3
	v_cvt_f32_i32_sdwa v26, sext(v57) dst_sel:DWORD dst_unused:UNUSED_PAD src0_sel:BYTE_0
	v_cvt_f32_i32_sdwa v27, sext(v57) dst_sel:DWORD dst_unused:UNUSED_PAD src0_sel:BYTE_1
	v_cvt_f32_i32_sdwa v28, sext(v57) dst_sel:DWORD dst_unused:UNUSED_PAD src0_sel:BYTE_2
	v_cvt_f32_i32_sdwa v29, sext(v57) dst_sel:DWORD dst_unused:UNUSED_PAD src0_sel:BYTE_3
	v_pk_fma_f32 v[16:17], v[30:31], v[2:3], v[16:17] op_sel_hi:[0,1,1]
	v_pk_fma_f32 v[14:15], v[30:31], v[22:23], v[14:15] op_sel_hi:[0,1,1]
	v_pk_fma_f32 v[12:13], v[30:31], v[26:27], v[12:13] op_sel_hi:[0,1,1]
	v_pk_fma_f32 v[10:11], v[30:31], v[28:29], v[10:11] op_sel_hi:[0,1,1]
	s_add_u32 s17, s15, 18
	v_readlane_b32 s28, v6, s17
	s_mul_i32 s29, s28, 0x220
	s_add_u32 s56, s26, s29
	s_addc_u32 s57, s27, 0
	global_load_dwordx2 v[56:57], v8, s[56:57]
	global_load_dword v30, v20, s[56:57] offset:512
	s_waitcnt vmcnt(18)
	v_cvt_f32_i32_sdwa v2, sext(v54) dst_sel:DWORD dst_unused:UNUSED_PAD src0_sel:BYTE_0
	v_cvt_f32_i32_sdwa v3, sext(v54) dst_sel:DWORD dst_unused:UNUSED_PAD src0_sel:BYTE_1
	v_cvt_f32_i32_sdwa v22, sext(v54) dst_sel:DWORD dst_unused:UNUSED_PAD src0_sel:BYTE_2
	v_cvt_f32_i32_sdwa v23, sext(v54) dst_sel:DWORD dst_unused:UNUSED_PAD src0_sel:BYTE_3
	v_cvt_f32_i32_sdwa v26, sext(v55) dst_sel:DWORD dst_unused:UNUSED_PAD src0_sel:BYTE_0
	v_cvt_f32_i32_sdwa v27, sext(v55) dst_sel:DWORD dst_unused:UNUSED_PAD src0_sel:BYTE_1
	v_cvt_f32_i32_sdwa v28, sext(v55) dst_sel:DWORD dst_unused:UNUSED_PAD src0_sel:BYTE_2
	v_cvt_f32_i32_sdwa v29, sext(v55) dst_sel:DWORD dst_unused:UNUSED_PAD src0_sel:BYTE_3
	v_pk_fma_f32 v[16:17], v[38:39], v[2:3], v[16:17] op_sel:[1,0,0] op_sel_hi:[1,1,1]
	v_pk_fma_f32 v[14:15], v[38:39], v[22:23], v[14:15] op_sel:[1,0,0] op_sel_hi:[1,1,1]
	v_pk_fma_f32 v[12:13], v[38:39], v[26:27], v[12:13] op_sel:[1,0,0] op_sel_hi:[1,1,1]
	v_pk_fma_f32 v[10:11], v[38:39], v[28:29], v[10:11] op_sel:[1,0,0] op_sel_hi:[1,1,1]
	s_add_u32 s17, s15, 17
	v_readlane_b32 s28, v6, s17
	s_mul_i32 s29, s28, 0x220
	s_add_u32 s54, s26, s29
	s_addc_u32 s55, s27, 0
	global_load_dwordx2 v[54:55], v8, s[54:55]
	global_load_dword v39, v20, s[54:55] offset:512
	s_waitcnt vmcnt(18)
	v_cvt_f32_i32_sdwa v2, sext(v52) dst_sel:DWORD dst_unused:UNUSED_PAD src0_sel:BYTE_0
	v_cvt_f32_i32_sdwa v3, sext(v52) dst_sel:DWORD dst_unused:UNUSED_PAD src0_sel:BYTE_1
	v_cvt_f32_i32_sdwa v22, sext(v52) dst_sel:DWORD dst_unused:UNUSED_PAD src0_sel:BYTE_2
	v_cvt_f32_i32_sdwa v23, sext(v52) dst_sel:DWORD dst_unused:UNUSED_PAD src0_sel:BYTE_3
	v_cvt_f32_i32_sdwa v26, sext(v53) dst_sel:DWORD dst_unused:UNUSED_PAD src0_sel:BYTE_0
	v_cvt_f32_i32_sdwa v27, sext(v53) dst_sel:DWORD dst_unused:UNUSED_PAD src0_sel:BYTE_1
	v_cvt_f32_i32_sdwa v28, sext(v53) dst_sel:DWORD dst_unused:UNUSED_PAD src0_sel:BYTE_2
	v_cvt_f32_i32_sdwa v29, sext(v53) dst_sel:DWORD dst_unused:UNUSED_PAD src0_sel:BYTE_3
	v_pk_fma_f32 v[16:17], v[38:39], v[2:3], v[16:17] op_sel_hi:[0,1,1]
	v_pk_fma_f32 v[14:15], v[38:39], v[22:23], v[14:15] op_sel_hi:[0,1,1]
	v_pk_fma_f32 v[12:13], v[38:39], v[26:27], v[12:13] op_sel_hi:[0,1,1]
	v_pk_fma_f32 v[10:11], v[38:39], v[28:29], v[10:11] op_sel_hi:[0,1,1]
	s_add_u32 s17, s15, 16
	v_readlane_b32 s28, v6, s17
	s_mul_i32 s29, s28, 0x220
	s_add_u32 s52, s26, s29
	s_addc_u32 s53, s27, 0
	global_load_dwordx2 v[52:53], v8, s[52:53]
	global_load_dword v38, v20, s[52:53] offset:512
	s_waitcnt vmcnt(18)
	v_cvt_f32_i32_sdwa v2, sext(v50) dst_sel:DWORD dst_unused:UNUSED_PAD src0_sel:BYTE_0
	v_cvt_f32_i32_sdwa v3, sext(v50) dst_sel:DWORD dst_unused:UNUSED_PAD src0_sel:BYTE_1
	v_cvt_f32_i32_sdwa v22, sext(v50) dst_sel:DWORD dst_unused:UNUSED_PAD src0_sel:BYTE_2
	v_cvt_f32_i32_sdwa v23, sext(v50) dst_sel:DWORD dst_unused:UNUSED_PAD src0_sel:BYTE_3
	v_cvt_f32_i32_sdwa v26, sext(v51) dst_sel:DWORD dst_unused:UNUSED_PAD src0_sel:BYTE_0
	v_cvt_f32_i32_sdwa v27, sext(v51) dst_sel:DWORD dst_unused:UNUSED_PAD src0_sel:BYTE_1
	v_cvt_f32_i32_sdwa v28, sext(v51) dst_sel:DWORD dst_unused:UNUSED_PAD src0_sel:BYTE_2
	v_cvt_f32_i32_sdwa v29, sext(v51) dst_sel:DWORD dst_unused:UNUSED_PAD src0_sel:BYTE_3
	v_pk_fma_f32 v[16:17], v[36:37], v[2:3], v[16:17] op_sel:[1,0,0] op_sel_hi:[1,1,1]
	v_pk_fma_f32 v[14:15], v[36:37], v[22:23], v[14:15] op_sel:[1,0,0] op_sel_hi:[1,1,1]
	v_pk_fma_f32 v[12:13], v[36:37], v[26:27], v[12:13] op_sel:[1,0,0] op_sel_hi:[1,1,1]
	v_pk_fma_f32 v[10:11], v[36:37], v[28:29], v[10:11] op_sel:[1,0,0] op_sel_hi:[1,1,1]
	s_add_u32 s17, s15, 15
	v_readlane_b32 s28, v6, s17
	s_mul_i32 s29, s28, 0x220
	s_add_u32 s50, s26, s29
	s_addc_u32 s51, s27, 0
	global_load_dwordx2 v[50:51], v8, s[50:51]
	global_load_dword v37, v20, s[50:51] offset:512
	s_waitcnt vmcnt(18)
	v_cvt_f32_i32_sdwa v2, sext(v48) dst_sel:DWORD dst_unused:UNUSED_PAD src0_sel:BYTE_0
	v_cvt_f32_i32_sdwa v3, sext(v48) dst_sel:DWORD dst_unused:UNUSED_PAD src0_sel:BYTE_1
	v_cvt_f32_i32_sdwa v22, sext(v48) dst_sel:DWORD dst_unused:UNUSED_PAD src0_sel:BYTE_2
	v_cvt_f32_i32_sdwa v23, sext(v48) dst_sel:DWORD dst_unused:UNUSED_PAD src0_sel:BYTE_3
	v_cvt_f32_i32_sdwa v26, sext(v49) dst_sel:DWORD dst_unused:UNUSED_PAD src0_sel:BYTE_0
	v_cvt_f32_i32_sdwa v27, sext(v49) dst_sel:DWORD dst_unused:UNUSED_PAD src0_sel:BYTE_1
	v_cvt_f32_i32_sdwa v28, sext(v49) dst_sel:DWORD dst_unused:UNUSED_PAD src0_sel:BYTE_2
	v_cvt_f32_i32_sdwa v29, sext(v49) dst_sel:DWORD dst_unused:UNUSED_PAD src0_sel:BYTE_3
	v_pk_fma_f32 v[16:17], v[36:37], v[2:3], v[16:17] op_sel_hi:[0,1,1]
	v_pk_fma_f32 v[14:15], v[36:37], v[22:23], v[14:15] op_sel_hi:[0,1,1]
	v_pk_fma_f32 v[12:13], v[36:37], v[26:27], v[12:13] op_sel_hi:[0,1,1]
	v_pk_fma_f32 v[10:11], v[36:37], v[28:29], v[10:11] op_sel_hi:[0,1,1]
	s_add_u32 s17, s15, 14
	v_readlane_b32 s28, v6, s17
	s_mul_i32 s29, s28, 0x220
	s_add_u32 s48, s26, s29
	s_addc_u32 s49, s27, 0
	global_load_dwordx2 v[48:49], v8, s[48:49]
	global_load_dword v36, v20, s[48:49] offset:512
	s_waitcnt vmcnt(18)
	v_cvt_f32_i32_sdwa v2, sext(v46) dst_sel:DWORD dst_unused:UNUSED_PAD src0_sel:BYTE_0
	v_cvt_f32_i32_sdwa v3, sext(v46) dst_sel:DWORD dst_unused:UNUSED_PAD src0_sel:BYTE_1
	v_cvt_f32_i32_sdwa v22, sext(v46) dst_sel:DWORD dst_unused:UNUSED_PAD src0_sel:BYTE_2
	v_cvt_f32_i32_sdwa v23, sext(v46) dst_sel:DWORD dst_unused:UNUSED_PAD src0_sel:BYTE_3
	v_cvt_f32_i32_sdwa v26, sext(v47) dst_sel:DWORD dst_unused:UNUSED_PAD src0_sel:BYTE_0
	v_cvt_f32_i32_sdwa v27, sext(v47) dst_sel:DWORD dst_unused:UNUSED_PAD src0_sel:BYTE_1
	v_cvt_f32_i32_sdwa v28, sext(v47) dst_sel:DWORD dst_unused:UNUSED_PAD src0_sel:BYTE_2
	v_cvt_f32_i32_sdwa v29, sext(v47) dst_sel:DWORD dst_unused:UNUSED_PAD src0_sel:BYTE_3
	v_pk_fma_f32 v[16:17], v[34:35], v[2:3], v[16:17] op_sel:[1,0,0] op_sel_hi:[1,1,1]
	v_pk_fma_f32 v[14:15], v[34:35], v[22:23], v[14:15] op_sel:[1,0,0] op_sel_hi:[1,1,1]
	v_pk_fma_f32 v[12:13], v[34:35], v[26:27], v[12:13] op_sel:[1,0,0] op_sel_hi:[1,1,1]
	v_pk_fma_f32 v[10:11], v[34:35], v[28:29], v[10:11] op_sel:[1,0,0] op_sel_hi:[1,1,1]
	s_add_u32 s17, s15, 13
	v_readlane_b32 s28, v6, s17
	s_mul_i32 s29, s28, 0x220
	s_add_u32 s46, s26, s29
	s_addc_u32 s47, s27, 0
	global_load_dwordx2 v[46:47], v8, s[46:47]
	global_load_dword v35, v20, s[46:47] offset:512
	s_waitcnt vmcnt(18)
	v_cvt_f32_i32_sdwa v2, sext(v44) dst_sel:DWORD dst_unused:UNUSED_PAD src0_sel:BYTE_0
	v_cvt_f32_i32_sdwa v3, sext(v44) dst_sel:DWORD dst_unused:UNUSED_PAD src0_sel:BYTE_1
	v_cvt_f32_i32_sdwa v22, sext(v44) dst_sel:DWORD dst_unused:UNUSED_PAD src0_sel:BYTE_2
	v_cvt_f32_i32_sdwa v23, sext(v44) dst_sel:DWORD dst_unused:UNUSED_PAD src0_sel:BYTE_3
	v_cvt_f32_i32_sdwa v26, sext(v45) dst_sel:DWORD dst_unused:UNUSED_PAD src0_sel:BYTE_0
	v_cvt_f32_i32_sdwa v27, sext(v45) dst_sel:DWORD dst_unused:UNUSED_PAD src0_sel:BYTE_1
	v_cvt_f32_i32_sdwa v28, sext(v45) dst_sel:DWORD dst_unused:UNUSED_PAD src0_sel:BYTE_2
	v_cvt_f32_i32_sdwa v29, sext(v45) dst_sel:DWORD dst_unused:UNUSED_PAD src0_sel:BYTE_3
	v_pk_fma_f32 v[16:17], v[34:35], v[2:3], v[16:17] op_sel_hi:[0,1,1]
	v_pk_fma_f32 v[14:15], v[34:35], v[22:23], v[14:15] op_sel_hi:[0,1,1]
	v_pk_fma_f32 v[12:13], v[34:35], v[26:27], v[12:13] op_sel_hi:[0,1,1]
	v_pk_fma_f32 v[10:11], v[34:35], v[28:29], v[10:11] op_sel_hi:[0,1,1]
	s_add_u32 s17, s15, 12
	v_readlane_b32 s28, v6, s17
	s_mul_i32 s29, s28, 0x220
	s_add_u32 s44, s26, s29
	s_addc_u32 s45, s27, 0
	global_load_dwordx2 v[44:45], v8, s[44:45]
	global_load_dword v34, v20, s[44:45] offset:512
	s_waitcnt vmcnt(18)
	v_cvt_f32_i32_sdwa v2, sext(v42) dst_sel:DWORD dst_unused:UNUSED_PAD src0_sel:BYTE_0
	v_cvt_f32_i32_sdwa v3, sext(v42) dst_sel:DWORD dst_unused:UNUSED_PAD src0_sel:BYTE_1
	v_cvt_f32_i32_sdwa v22, sext(v42) dst_sel:DWORD dst_unused:UNUSED_PAD src0_sel:BYTE_2
	v_cvt_f32_i32_sdwa v23, sext(v42) dst_sel:DWORD dst_unused:UNUSED_PAD src0_sel:BYTE_3
	v_cvt_f32_i32_sdwa v26, sext(v43) dst_sel:DWORD dst_unused:UNUSED_PAD src0_sel:BYTE_0
	v_cvt_f32_i32_sdwa v27, sext(v43) dst_sel:DWORD dst_unused:UNUSED_PAD src0_sel:BYTE_1
	v_cvt_f32_i32_sdwa v28, sext(v43) dst_sel:DWORD dst_unused:UNUSED_PAD src0_sel:BYTE_2
	v_cvt_f32_i32_sdwa v29, sext(v43) dst_sel:DWORD dst_unused:UNUSED_PAD src0_sel:BYTE_3
	v_pk_fma_f32 v[16:17], v[32:33], v[2:3], v[16:17] op_sel:[1,0,0] op_sel_hi:[1,1,1]
	v_pk_fma_f32 v[14:15], v[32:33], v[22:23], v[14:15] op_sel:[1,0,0] op_sel_hi:[1,1,1]
	v_pk_fma_f32 v[12:13], v[32:33], v[26:27], v[12:13] op_sel:[1,0,0] op_sel_hi:[1,1,1]
	v_pk_fma_f32 v[10:11], v[32:33], v[28:29], v[10:11] op_sel:[1,0,0] op_sel_hi:[1,1,1]
	s_add_u32 s17, s15, 11
	v_readlane_b32 s28, v6, s17
	s_mul_i32 s29, s28, 0x220
	s_add_u32 s42, s26, s29
	s_addc_u32 s43, s27, 0
	global_load_dwordx2 v[42:43], v8, s[42:43]
	global_load_dword v33, v20, s[42:43] offset:512
	s_waitcnt vmcnt(18)
	v_cvt_f32_i32_sdwa v2, sext(v40) dst_sel:DWORD dst_unused:UNUSED_PAD src0_sel:BYTE_0
	v_cvt_f32_i32_sdwa v3, sext(v40) dst_sel:DWORD dst_unused:UNUSED_PAD src0_sel:BYTE_1
	v_cvt_f32_i32_sdwa v22, sext(v40) dst_sel:DWORD dst_unused:UNUSED_PAD src0_sel:BYTE_2
	v_cvt_f32_i32_sdwa v23, sext(v40) dst_sel:DWORD dst_unused:UNUSED_PAD src0_sel:BYTE_3
	v_cvt_f32_i32_sdwa v26, sext(v41) dst_sel:DWORD dst_unused:UNUSED_PAD src0_sel:BYTE_0
	v_cvt_f32_i32_sdwa v27, sext(v41) dst_sel:DWORD dst_unused:UNUSED_PAD src0_sel:BYTE_1
	v_cvt_f32_i32_sdwa v28, sext(v41) dst_sel:DWORD dst_unused:UNUSED_PAD src0_sel:BYTE_2
	v_cvt_f32_i32_sdwa v29, sext(v41) dst_sel:DWORD dst_unused:UNUSED_PAD src0_sel:BYTE_3
	v_pk_fma_f32 v[16:17], v[32:33], v[2:3], v[16:17] op_sel_hi:[0,1,1]
	v_pk_fma_f32 v[14:15], v[32:33], v[22:23], v[14:15] op_sel_hi:[0,1,1]
	v_pk_fma_f32 v[12:13], v[32:33], v[26:27], v[12:13] op_sel_hi:[0,1,1]
	v_pk_fma_f32 v[10:11], v[32:33], v[28:29], v[10:11] op_sel_hi:[0,1,1]
	s_add_u32 s17, s15, 10
	v_readlane_b32 s28, v6, s17
	s_mul_i32 s29, s28, 0x220
	s_add_u32 s40, s26, s29
	s_addc_u32 s41, s27, 0
	global_load_dwordx2 v[40:41], v8, s[40:41]
	global_load_dword v32, v20, s[40:41] offset:512
	s_add_u32 s15, s15, 10
	s_mov_b32 s16, 10
	s_branch .Lagg_chk
